# stagger: workgroup group (wgid>>3)&3 delayed by g*s_sleep47 at the start of multi-unit GEMM phases so epilogue store bursts of different CUs do not coincide
# baseline (speedup 1.0000x reference)
.LBB0_165:
	v_and_b32_e32 v11, 15, v1
	v_bfe_u32 v10, v1, 4, 2
	v_lshl_or_b32 v1, s8, 6, v11
	v_lshlrev_b32_e32 v8, 4, v10
	v_lshlrev_b32_e32 v13, 2, v1
	s_and_b32 s16, s50, 3
	v_lshl_or_b32 v8, v11, 6, v8
	s_lshl_b32 s14, s8, 13
	v_and_b32_e32 v9, 32, v13
	s_waitcnt vmcnt(0)
	v_bitop3_b32 v14, v8, s14, v9 bitop3:0xde
	s_lshl_b32 s14, s16, 12
	s_and_b64 s[38:39], s[40:41], exec
	s_cselect_b32 s75, 0, 2
	s_add_u32 s84, s42, 0x30100000
	s_addc_u32 s85, s43, 0
	s_add_u32 s17, s42, 0x3a100000
	s_addc_u32 s26, s43, 0
	s_and_b64 s[38:39], s[40:41], exec
	v_lshlrev_b32_e32 v15, 2, v11
	s_cselect_b32 s47, s26, 0
	s_cselect_b32 s46, s17, 0
	s_add_u32 s38, s64, 0x8000
	v_mov_b32_e32 v151, v115
	v_and_b32_e32 v9, 32, v15
	s_addc_u32 s39, s65, 0
	v_bitop3_b32 v182, v8, s14, v9 bitop3:0xde
	s_add_i32 m0, s37, 0x18000
	v_lshl_add_u64 v[8:9], s[38:39], 0, v[150:151]
	v_mov_b32_e32 v155, v115
	s_waitcnt vmcnt(2)
	s_barrier
	global_load_lds_dwordx4 v[8:9], off
	s_add_i32 m0, s37, 0x1a000
	v_lshl_add_u64 v[8:9], s[38:39], 0, v[154:155]
	s_add_u32 s38, s62, 0x8000
	v_mov_b32_e32 v149, v115
	s_addc_u32 s39, s63, 0
	s_add_i32 s86, s37, 0x8000
	v_mov_b32_e32 v153, v115
	global_load_lds_dwordx4 v[8:9], off
	v_lshl_add_u64 v[8:9], s[38:39], 0, v[148:149]
	s_mov_b32 m0, s86
	s_add_i32 s87, s37, 0xa000
	global_load_lds_dwordx4 v[8:9], off
	v_lshl_add_u64 v[8:9], s[38:39], 0, v[152:153]
	s_add_u32 s38, s64, 0x9000
	s_mov_b32 m0, s87
	s_addc_u32 s39, s65, 0
	global_load_lds_dwordx4 v[8:9], off
	s_add_i32 m0, s37, 0x1c000
	v_lshl_add_u64 v[8:9], s[38:39], 0, v[150:151]
	global_load_lds_dwordx4 v[8:9], off
	v_lshl_add_u64 v[8:9], s[38:39], 0, v[154:155]
	s_add_i32 m0, s37, 0x1e000
	s_cmpk_lt_u32 s15, 0x100
	global_load_lds_dwordx4 v[8:9], off
	v_or_b32_e32 v8, 16, v1
	v_lshlrev_b32_e32 v17, 4, v8
	v_or_b32_e32 v9, 32, v1
	v_lshlrev_b32_e32 v8, 2, v8
	v_or_b32_e32 v19, 48, v1
	v_bitop3_b32 v29, v8, 1, s16 bitop3:0x36
	v_lshlrev_b32_e32 v8, 2, v9
	s_cselect_b64 s[48:49], -1, 0
	v_add_u32_e32 v21, 0x80, v1
	v_bitop3_b32 v30, v8, 1, s16 bitop3:0x36
	v_lshlrev_b32_e32 v8, 2, v19
	s_lshl_b32 s15, s50, 8
	v_lshlrev_b32_e32 v20, 4, v19
	v_add_u32_e32 v23, 0x90, v1
	s_bfe_u32 s88, s50, 0x10001
	v_bitop3_b32 v19, v8, 1, s16 bitop3:0x36
	v_lshlrev_b32_e32 v8, 2, v21
	s_and_b32 s15, s15, 0x100
	v_lshlrev_b32_e32 v22, 4, v21
	v_add_u32_e32 v25, 0xa0, v1
	v_bitop3_b32 v21, v8, 1, s16 bitop3:0x36
	v_lshlrev_b32_e32 v8, 2, v23
	s_add_u32 s42, s42, s15
	v_lshlrev_b32_e32 v24, 4, v23
	v_add_u32_e32 v27, 0xb0, v1
	v_bitop3_b32 v23, v8, 1, s16 bitop3:0x36
	v_lshlrev_b32_e32 v8, 2, v25
	s_addc_u32 s43, s43, 0
	v_lshlrev_b32_e32 v26, 4, v25
	v_bitop3_b32 v25, v8, 1, s16 bitop3:0x36
	v_lshlrev_b32_e32 v8, 2, v27
	v_lshlrev_b32_e32 v114, 5, v10
	s_cmp_lg_u64 s[46:47], 0
	v_lshlrev_b32_e32 v18, 4, v9
	v_lshlrev_b32_e32 v28, 4, v27
	v_bitop3_b32 v27, v8, 1, s16 bitop3:0x36
	v_lshl_add_u64 v[8:9], s[42:43], 0, v[114:115]
	s_mov_b64 s[26:27], 0x36100000
	s_cselect_b64 s[50:51], -1, 0
	s_mov_b64 s[42:43], 0x3e104000
	s_abs_i32 s89, s4
	v_lshl_add_u64 v[166:167], v[8:9], 0, s[26:27]
	v_lshl_add_u64 v[168:169], v[8:9], 0, s[42:43]
	v_cvt_f32_u32_e32 v8, s89
	v_lshlrev_b32_e32 v12, 3, v10
	v_cmp_eq_u32_e64 s[40:41], 0, v11
	v_bitop3_b32 v11, v13, 1, s16 bitop3:0x36
	v_rcp_iflag_f32_e32 v8, v8
	s_lshl_b32 s15, s16, 2
	v_lshl_or_b32 v209, s16, 6, v12
	v_readlane_b32 s17, v255, 5
	v_mul_f32_e32 v8, 0x4f7ffffe, v8
	v_cvt_u32_f32_e32 v8, v8
	v_lshlrev_b32_e32 v16, 4, v1
	s_add_i32 s15, s17, s15
	v_add_u32_e32 v183, s15, v16
	v_readfirstlane_b32 s16, v8
	v_lshlrev_b32_e32 v8, 10, v2
	v_and_b32_e32 v8, 0xfffff800, v8
	v_lshl_add_u32 v3, v3, 7, v8
	v_and_b32_e32 v2, 1, v2
	v_add_u32_e32 v195, s15, v17
	v_add_u32_e32 v197, s15, v18
	v_add_u32_e32 v199, s15, v20
	v_add_u32_e32 v201, s15, v22
	v_add_u32_e32 v203, s15, v24
	v_add_u32_e32 v205, s15, v26
	v_add_u32_e32 v207, s15, v28
	s_sub_i32 s15, 0, s89
	v_lshl_or_b32 v2, v2, 6, v3
	s_mul_i32 s15, s15, s16
	v_lshl_add_u32 v170, v4, 1, v2
	v_lshlrev_b32_e32 v2, 10, v5
	s_mul_hi_u32 s15, s16, s15
	v_and_b32_e32 v2, 0xfffff800, v2
	s_waitcnt vmcnt(6)
	s_add_i32 s93, s16, s15
	s_lshl_b32 s15, s8, 8
	v_readlane_b32 s16, v255, 4
	v_lshl_add_u32 v2, v6, 7, v2
	v_and_b32_e32 v3, 1, v5
	s_add_i32 s15, s16, s15
	v_lshl_or_b32 v2, v3, 6, v2
	s_mov_b32 s14, 0
	v_cmp_eq_u32_e64 s[38:39], 0, v10
	v_lshl_add_u32 v194, v11, 2, s17
	v_lshl_add_u32 v196, v29, 2, s17
	v_lshl_add_u32 v198, v30, 2, s17
	v_lshl_add_u32 v200, v19, 2, s17
	v_lshl_add_u32 v202, v21, 2, s17
	v_lshl_add_u32 v204, v23, 2, s17
	v_lshl_add_u32 v206, v25, 2, s17
	v_lshl_add_u32 v208, v27, 2, s17
	s_ashr_i32 s92, s4, 31
	v_add_u32_e32 v210, s15, v15
	v_add_u32_e32 v211, s16, v13
	v_mov_b32_e32 v171, v115
	v_lshl_add_u32 v172, v7, 1, v2
	v_mov_b32_e32 v173, v115
	v_add_u32_e32 v212, 0, v14
	s_mov_b32 s94, 0
	s_barrier
	v_readlane_b32 s100, v254, 0
	s_nop 3
	s_bfe_u32 s100, s100, 0x20003
	s_cmp_eq_u32 s100, 0
	s_cbranch_scc1 .Lstg_done_split
.Lstg_loop_split:
	s_sleep 47
	s_sub_u32 s100, s100, 1
	s_cmp_lg_u32 s100, 0
	s_cbranch_scc1 .Lstg_loop_split
.Lstg_done_split:
	s_branch .LBB0_168
.LBB0_166:
	s_mov_b64 s[28:29], 0

.LBB0_336:
	s_and_b32 s16, s37, 3
	s_lshl_b32 s17, s15, 13
	s_lshl_b32 s29, s16, 12
	s_add_u32 s37, s44, 0x1a100000
	s_addc_u32 s64, s45, 0
	s_add_u32 s42, s44, 0x22100000
	s_addc_u32 s43, s45, 0
	s_add_u32 s44, s44, 0x3e102000
	s_addc_u32 s45, s45, 0
	s_add_u32 s38, s58, 0x8000
	v_mov_b32_e32 v143, v115
	s_addc_u32 s39, s59, 0
	s_add_i32 m0, s13, 0x18000
	v_lshl_add_u64 v[10:11], s[38:39], 0, v[142:143]
	v_mov_b32_e32 v147, v115
	s_waitcnt vmcnt(2)
	s_barrier
	global_load_lds_dwordx4 v[10:11], off
	s_add_i32 m0, s13, 0x1a000
	v_lshl_add_u64 v[10:11], s[38:39], 0, v[146:147]
	s_add_u32 s38, s56, 0x8000
	v_mov_b32_e32 v141, v115
	s_addc_u32 s39, s57, 0
	s_add_i32 s65, s13, 0x8000
	v_mov_b32_e32 v145, v115
	global_load_lds_dwordx4 v[10:11], off
	v_lshl_add_u64 v[10:11], s[38:39], 0, v[140:141]
	s_mov_b32 m0, s65
	s_add_i32 s66, s13, 0xa000
	global_load_lds_dwordx4 v[10:11], off
	v_lshl_add_u64 v[10:11], s[38:39], 0, v[144:145]
	s_add_u32 s38, s58, 0x9000
	s_mov_b32 m0, s66
	s_addc_u32 s39, s59, 0
	global_load_lds_dwordx4 v[10:11], off
	s_add_i32 m0, s13, 0x1c000
	v_lshl_add_u64 v[10:11], s[38:39], 0, v[142:143]
	global_load_lds_dwordx4 v[10:11], off
	v_lshl_add_u64 v[10:11], s[38:39], 0, v[146:147]
	s_add_i32 m0, s13, 0x1e000
	v_and_b32_e32 v9, 15, v2
	global_load_lds_dwordx4 v[10:11], off
	v_lshrrev_b32_e32 v2, 1, v2
	v_and_b32_e32 v2, 24, v2
	v_lshlrev_b32_e32 v10, 1, v2
	v_lshl_or_b32 v173, s16, 6, v2
	v_lshlrev_b32_e32 v2, 10, v3
	v_and_b32_e32 v2, 0xfffff800, v2
	v_lshl_add_u32 v2, v4, 7, v2
	v_and_b32_e32 v3, 1, v3
	v_lshl_or_b32 v2, v3, 6, v2
	s_cmpk_lt_u32 s14, 0x100
	v_lshl_add_u32 v148, v5, 1, v2
	v_lshlrev_b32_e32 v2, 10, v6
	v_lshl_or_b32 v1, s15, 6, v9
	v_lshl_or_b32 v10, v9, 6, v10
	v_lshlrev_b32_e32 v9, 2, v9
	s_cselect_b64 s[46:47], -1, 0
	s_lshl_b32 s14, s15, 8
	v_and_b32_e32 v2, 0xfffff800, v2
	v_and_b32_e32 v11, 32, v9
	s_waitcnt vmcnt(6)
	s_add_i32 s14, s14, 0
	v_lshl_add_u32 v2, v7, 7, v2
	v_and_b32_e32 v3, 1, v6
	v_bitop3_b32 v12, v10, s17, v11 bitop3:0xde
	s_add_i32 s14, s14, 0x20400
	v_lshl_or_b32 v2, v3, 6, v2
	v_bitop3_b32 v172, v10, s29, v11 bitop3:0xde
	v_add_u32_e32 v174, s14, v9
	v_mov_b32_e32 v149, v115
	v_lshl_add_u32 v150, v8, 1, v2
	v_mov_b32_e32 v151, v115
	s_mov_b32 s14, 0
	v_add_u32_e32 v175, 0, v12
	s_mov_b32 s67, 0
	s_barrier
	v_readlane_b32 s100, v254, 0
	s_nop 3
	s_bfe_u32 s100, s100, 0x20003
	s_cmp_eq_u32 s100, 0
	s_cbranch_scc1 .Lstg_done_hgrn1

.Lstg_done_hgrn1:
	s_branch .LBB0_339
.LBB0_337:
	s_mov_b64 s[28:29], 0

.LBB0_493:
	s_and_b32 s16, s24, 3
	s_lshl_b32 s17, s15, 13
	s_lshl_b32 s29, s16, 12
	s_add_u32 s24, s50, 0x1a100000
	s_addc_u32 s37, s51, 0
	s_add_u32 s26, s50, 0x22100000
	s_addc_u32 s27, s51, 0
	s_add_u32 s42, s50, 0x3e100000
	s_addc_u32 s43, s51, 0
	s_add_u32 s38, s56, 0x8000
	v_mov_b32_e32 v143, v115
	s_addc_u32 s39, s57, 0
	s_add_i32 m0, s12, 0x18000
	v_lshl_add_u64 v[10:11], s[38:39], 0, v[142:143]
	v_mov_b32_e32 v147, v115
	s_waitcnt vmcnt(2)
	s_barrier
	global_load_lds_dwordx4 v[10:11], off
	s_add_i32 m0, s12, 0x1a000
	v_lshl_add_u64 v[10:11], s[38:39], 0, v[146:147]
	s_add_u32 s38, s54, 0x8000
	v_mov_b32_e32 v141, v115
	s_addc_u32 s39, s55, 0
	s_add_i32 s62, s12, 0x8000
	v_mov_b32_e32 v145, v115
	global_load_lds_dwordx4 v[10:11], off
	v_lshl_add_u64 v[10:11], s[38:39], 0, v[140:141]
	s_mov_b32 m0, s62
	s_add_i32 s63, s12, 0xa000
	global_load_lds_dwordx4 v[10:11], off
	v_lshl_add_u64 v[10:11], s[38:39], 0, v[144:145]
	s_add_u32 s38, s56, 0x9000
	s_mov_b32 m0, s63
	s_addc_u32 s39, s57, 0
	global_load_lds_dwordx4 v[10:11], off
	s_add_i32 m0, s12, 0x1c000
	v_lshl_add_u64 v[10:11], s[38:39], 0, v[142:143]
	global_load_lds_dwordx4 v[10:11], off
	v_lshl_add_u64 v[10:11], s[38:39], 0, v[146:147]
	s_add_i32 m0, s12, 0x1e000
	v_and_b32_e32 v9, 15, v2
	global_load_lds_dwordx4 v[10:11], off
	v_lshrrev_b32_e32 v2, 1, v2
	v_and_b32_e32 v2, 24, v2
	v_lshlrev_b32_e32 v10, 1, v2
	v_lshl_or_b32 v173, s16, 6, v2
	v_lshlrev_b32_e32 v2, 10, v3
	v_and_b32_e32 v2, 0xfffff800, v2
	v_lshl_add_u32 v2, v4, 7, v2
	v_and_b32_e32 v3, 1, v3
	v_lshl_or_b32 v2, v3, 6, v2
	s_cmpk_lt_u32 s14, 0x100
	v_lshl_add_u32 v148, v5, 1, v2
	v_lshlrev_b32_e32 v2, 10, v6
	v_lshl_or_b32 v1, s15, 6, v9
	v_lshl_or_b32 v10, v9, 6, v10
	v_lshlrev_b32_e32 v9, 2, v9
	s_cselect_b64 s[44:45], -1, 0
	s_lshl_b32 s14, s15, 8
	v_and_b32_e32 v2, 0xfffff800, v2
	v_and_b32_e32 v11, 32, v9
	s_waitcnt vmcnt(6)
	s_add_i32 s14, s14, 0
	v_lshl_add_u32 v2, v7, 7, v2
	v_and_b32_e32 v3, 1, v6
	v_bitop3_b32 v12, v10, s17, v11 bitop3:0xde
	s_add_i32 s14, s14, 0x20400
	v_lshl_or_b32 v2, v3, 6, v2
	v_bitop3_b32 v172, v10, s29, v11 bitop3:0xde
	v_add_u32_e32 v174, s14, v9
	v_mov_b32_e32 v149, v115
	v_lshl_add_u32 v150, v8, 1, v2
	v_mov_b32_e32 v151, v115
	s_mov_b32 s14, 0
	v_add_u32_e32 v175, 0, v12
	s_mov_b32 s64, 0
	s_barrier
	v_readlane_b32 s100, v254, 0
	s_nop 3
	s_bfe_u32 s100, s100, 0x20003
	s_cmp_eq_u32 s100, 0
	s_cbranch_scc1 .Lstg_done_hgrn2

.Lstg_done_hgrn2:
	s_branch .LBB0_496
.LBB0_494:
	s_mov_b64 s[28:29], 0

.LBB0_1220:
	v_and_b32_e32 v9, 15, v1
	v_and_b32_e32 v8, 48, v1
	v_lshlrev_b32_e32 v12, 2, v9
	s_sext_i32_i8 s58, s10
	s_and_b32 s45, s29, 3
	v_lshl_or_b32 v1, v9, 6, v8
	s_lshl_b32 s10, s28, 13
	v_and_b32_e32 v10, 32, v12
	s_lshl_b32 s29, s28, 6
	v_bitop3_b32 v13, v1, s10, v10 bitop3:0xde
	s_lshl_b32 s10, s45, 12
	s_add_u32 s16, s48, 0x8000
	s_addc_u32 s17, s49, 0
	v_bitop3_b32 v1, v1, s10, v10 bitop3:0xde
	s_add_i32 m0, s20, 0x18000
	v_lshl_add_u64 v[10:11], s[16:17], 0, v[114:115]
	v_mov_b32_e32 v137, v115
	s_waitcnt vmcnt(2)
	s_barrier
	global_load_lds_dwordx4 v[10:11], off
	s_add_i32 m0, s20, 0x1a000
	v_lshl_add_u64 v[10:11], s[16:17], 0, v[136:137]
	s_add_u32 s16, s46, 0x8000
	v_mov_b32_e32 v133, v115
	s_addc_u32 s17, s47, 0
	s_add_i32 s54, s20, 0x8000
	v_mov_b32_e32 v135, v115
	global_load_lds_dwordx4 v[10:11], off
	v_lshl_add_u64 v[10:11], s[16:17], 0, v[132:133]
	s_mov_b32 m0, s54
	s_add_i32 s55, s20, 0xa000
	global_load_lds_dwordx4 v[10:11], off
	v_lshl_add_u64 v[10:11], s[16:17], 0, v[134:135]
	s_add_u32 s16, s48, 0x9000
	s_mov_b32 m0, s55
	s_addc_u32 s17, s49, 0
	global_load_lds_dwordx4 v[10:11], off
	s_add_i32 m0, s20, 0x1c000
	v_lshl_add_u64 v[10:11], s[16:17], 0, v[114:115]
	global_load_lds_dwordx4 v[10:11], off
	v_lshl_add_u64 v[10:11], s[16:17], 0, v[136:137]
	s_add_i32 m0, s20, 0x1e000
	s_cmpk_lt_u32 s11, 0x100
	global_load_lds_dwordx4 v[10:11], off
	s_cselect_b64 s[10:11], -1, 0
	s_ashr_i32 s16, s29, 31
	v_or_b32_e32 v10, s29, v9
	v_mov_b32_e32 v11, s16
	v_lshlrev_b64 v[10:11], 7, v[10:11]
	v_lshl_add_u64 v[10:11], s[26:27], 0, v[10:11]
	v_mov_b32_e32 v9, v115
	v_lshl_add_u64 v[8:9], v[10:11], 0, v[8:9]
	s_mov_b64 s[16:17], 0x28100000
	v_lshl_add_u64 v[138:139], v[8:9], 0, s[16:17]
	v_lshlrev_b32_e32 v8, 10, v2
	v_and_b32_e32 v8, 0xfffff800, v8
	v_lshl_add_u32 v3, v3, 7, v8
	v_and_b32_e32 v2, 1, v2
	v_lshl_or_b32 v2, v2, 6, v3
	v_lshl_add_u32 v140, v4, 1, v2
	v_lshlrev_b32_e32 v2, 10, v5
	s_lshl_b32 s16, s28, 8
	v_and_b32_e32 v2, 0xfffff800, v2
	s_waitcnt vmcnt(6)
	s_add_i32 s16, s16, 0
	v_lshl_add_u32 v2, v6, 7, v2
	v_and_b32_e32 v3, 1, v5
	s_add_i32 s16, s16, 0x20400
	v_lshl_or_b32 v2, v3, 6, v2
	v_add_u32_e32 v146, s16, v12
	v_mov_b32_e32 v141, v115
	v_lshl_add_u32 v142, v7, 1, v2
	v_mov_b32_e32 v143, v115
	s_mov_b32 s59, 0
	v_add_u32_e32 v147, 0, v13
	s_mov_b32 s56, 0
	s_barrier
	s_waitcnt vmcnt(0)
	v_readlane_b32 s100, v254, 0
	s_nop 3
	s_bfe_u32 s100, s100, 0x20003
	s_cmp_eq_u32 s100, 0
	s_cbranch_scc1 .Lstg_done_relu2

.Lstg_done_relu2:
	s_branch .LBB0_1223
.LBB0_1221:
	s_mov_b64 s[38:39], 0
